# v31: v29 + combine3 loop: second row's expert-output loads issued right behind the first row's (free registers), not after the first row's stores
# baseline (speedup 1.0000x reference)
.LBB0_3130:
	s_add_i32 s4, s0, s8
	s_cmpk_lt_i32 s4, 0x4000
	s_cselect_b32 s4, s4, s8
	s_ashr_i32 s27, s26, 31
	s_add_i32 s30, s26, 1
	s_ashr_i32 s31, s30, 31
	s_lshl_b64 s[48:49], s[26:27], 2
	s_add_u32 s34, s36, s48
	s_addc_u32 s35, s37, s49
	v_mbcnt_lo_u32_b32 v16, -1, 0
	v_mbcnt_hi_u32_b32 v16, -1, v16
	global_load_dwordx2 v[72:73], v78, s[34:35]
	s_add_u32 s34, s38, s48
	s_addc_u32 s35, s39, s49
	s_lshl_b64 s[50:51], s[30:31], 2
	s_add_u32 s30, s38, s50
	v_lshlrev_b32_e32 v36, 4, v16
	s_addc_u32 s31, s39, s51
	v_ashrrev_i32_e32 v37, 31, v36
	global_load_dword v74, v78, s[34:35]
	global_load_dword v76, v78, s[30:31]
	s_add_u32 s30, s40, s6
	v_lshlrev_b64 v[16:17], 1, v[36:37]
	s_addc_u32 s31, s41, s7
	v_lshl_add_u64 v[20:21], s[12:13], 0, v[16:17]
	v_lshl_add_u64 v[16:17], s[30:31], 0, v[16:17]
	s_add_u32 s30, s9, s6
	s_addc_u32 s31, s42, s7
	v_add_co_u32_e32 v38, vcc, s43, v16
	s_lshl_b32 s34, s4, 1
	v_lshl_add_u64 v[22:23], v[16:17], 0, s[10:11]
	v_addc_co_u32_e32 v39, vcc, 0, v17, vcc
	v_lshl_add_u64 v[16:17], v[16:17], 0, s[28:29]
	s_ashr_i32 s35, s34, 31
	global_load_dwordx4 v[40:43], v[38:39], off
	global_load_dwordx4 v[44:47], v[22:23], off offset:16
	global_load_dwordx4 v[48:51], v[38:39], off offset:2048
	global_load_dwordx4 v[52:55], v[16:17], off offset:16
	v_lshl_add_u64 v[16:17], s[30:31], 0, v[36:37]
	s_lshl_b64 s[34:35], s[34:35], 2
	v_add_co_u32_e32 v16, vcc, s44, v16
	s_add_u32 s52, s1, s34
	s_nop 0
	v_addc_co_u32_e32 v17, vcc, 0, v17, vcc
	s_addc_u32 s53, s33, s35
	global_load_dwordx4 v[56:59], v[16:17], off
	global_load_dwordx4 v[60:63], v[16:17], off offset:1024
	global_load_dwordx2 v[98:99], v78, s[52:53]
	s_add_u32 s52, s36, s34
	s_addc_u32 s53, s37, s35
	s_add_u32 s34, s38, s34
	s_addc_u32 s35, s39, s35
	s_ashr_i32 s5, s4, 31
	s_and_b32 s27, s26, 0xffffe000
	global_load_dwordx2 v[34:35], v78, s[52:53]
	global_load_dwordx2 v[100:101], v78, s[34:35]
	s_lshl_b64 s[34:35], s[4:5], 11
	s_lshl_b64 s[4:5], s[4:5], 12
	s_add_i32 s27, s27, 0
	v_lshl_add_u64 v[18:19], s[14:15], 0, v[36:37]
	v_lshl_add_u64 v[32:33], v[20:21], 0, s[4:5]
	s_add_u32 s4, s1, s50
	v_lshl_add_u64 v[16:17], v[18:19], 0, s[34:35]
	v_add_u32_e32 v81, s27, v36
	global_load_dwordx4 v[64:67], v[32:33], off offset:16
	global_load_dwordx4 v[68:71], v[32:33], off
	global_load_dwordx4 v[82:85], v[32:33], off offset:2064
	global_load_dwordx4 v[86:89], v[32:33], off offset:2048
	global_load_dwordx4 v[90:93], v[16:17], off
	global_load_dwordx4 v[94:97], v[16:17], off offset:1024
	s_addc_u32 s5, s33, s51
	ds_read_b128 v[28:31], v81
	ds_read_b128 v[24:27], v81 offset:1024
	ds_read_b128 v[20:23], v81 offset:2048
	ds_read_b128 v[16:19], v81 offset:3072
	global_load_dword v158, v78, s[4:5]
	s_add_u32 s4, s1, s48
	s_addc_u32 s5, s33, s49
	global_load_dword v159, v78, s[4:5]
	v_mov_b32_e32 v0, 0
	v_mov_b32_e32 v1, 0
	v_mov_b32_e32 v2, 0
	v_mov_b32_e32 v3, 0
	v_mov_b32_e32 v4, 0
	v_mov_b32_e32 v5, 0
	v_mov_b32_e32 v6, 0
	v_mov_b32_e32 v7, 0
	v_mov_b32_e32 v8, 0
	v_mov_b32_e32 v9, 0
	v_mov_b32_e32 v10, 0
	v_mov_b32_e32 v11, 0
	v_mov_b32_e32 v12, 0
	v_mov_b32_e32 v13, 0
	v_mov_b32_e32 v14, 0
	v_mov_b32_e32 v15, 0
	s_add_i32 s8, s8, s20
	s_add_u32 s40, s40, s22
	s_addc_u32 s41, s41, s23
	s_add_u32 s9, s9, s24
	s_addc_u32 s42, s42, s25
	s_add_i32 s26, s26, s21
	s_cmpk_lt_i32 s8, 0x4000
	s_waitcnt vmcnt(18)
	v_ashrrev_i32_e32 v75, 31, v74
	s_waitcnt vmcnt(17)
	v_ashrrev_i32_e32 v77, 31, v76
	v_lshlrev_b64 v[102:103], 11, v[74:75]
	v_lshlrev_b64 v[104:105], 11, v[76:77]
	s_waitcnt vmcnt(16)
	v_lshlrev_b32_e32 v74, 16, v40
	s_waitcnt vmcnt(15)
	v_lshlrev_b32_e32 v108, 16, v46
	v_and_b32_e32 v109, 0xffff0000, v46
	s_waitcnt vmcnt(14)
	v_lshlrev_b32_e32 v110, 16, v48
	v_and_b32_e32 v111, 0xffff0000, v48
	v_lshlrev_b32_e32 v48, 16, v49
	v_and_b32_e32 v49, 0xffff0000, v49
	s_waitcnt vmcnt(13)
	v_lshlrev_b32_e32 v114, 16, v52
	v_and_b32_e32 v115, 0xffff0000, v52
	v_lshlrev_b32_e32 v52, 16, v53
	v_and_b32_e32 v53, 0xffff0000, v53
	s_waitcnt vmcnt(12)
	v_cvt_pk_f32_fp8_e32 v[128:129], v59
	s_waitcnt vmcnt(11)
	v_cvt_pk_f32_fp8_sdwa v[132:133], v60 src0_sel:WORD_1
	v_cvt_pk_f32_fp8_sdwa v[138:139], v62 src0_sel:WORD_1
	v_cvt_pk_f32_fp8_e32 v[118:119], v56
	v_cvt_pk_f32_fp8_sdwa v[120:121], v56 src0_sel:WORD_1
	v_cvt_pk_f32_fp8_e32 v[122:123], v57
	v_cvt_pk_f32_fp8_sdwa v[56:57], v57 src0_sel:WORD_1
	v_cvt_pk_f32_fp8_e32 v[124:125], v58
	v_cvt_pk_f32_fp8_sdwa v[126:127], v58 src0_sel:WORD_1
	v_cvt_pk_f32_fp8_sdwa v[58:59], v59 src0_sel:WORD_1
	v_pk_add_f32 v[108:109], v[128:129], v[108:109]
	v_pk_add_f32 v[128:129], v[132:133], v[48:49]
	v_pk_add_f32 v[132:133], v[138:139], v[52:53]
	v_and_b32_e32 v75, 0xffff0000, v40
	v_lshlrev_b32_e32 v40, 16, v41
	v_and_b32_e32 v41, 0xffff0000, v41
	v_lshlrev_b32_e32 v76, 16, v42
	v_and_b32_e32 v77, 0xffff0000, v42
	s_waitcnt vmcnt(3)
	v_cvt_pk_f32_fp8_e32 v[52:53], v91
	s_waitcnt vmcnt(2)
	v_cvt_pk_f32_fp8_sdwa v[152:153], v96 src0_sel:WORD_1
	v_lshlrev_b32_e32 v42, 16, v43
	v_and_b32_e32 v43, 0xffff0000, v43
	v_lshlrev_b32_e32 v98, 2, v98
	v_lshlrev_b32_e32 v99, 2, v99
	v_cvt_pk_f32_fp8_e32 v[134:135], v61
	v_cvt_pk_f32_fp8_e32 v[136:137], v62
	v_cvt_pk_f32_fp8_e32 v[140:141], v63
	v_cvt_pk_f32_fp8_sdwa v[62:63], v63 src0_sel:WORD_1
	v_add_u32_e32 v178, s45, v98
	v_add_u32_e32 v179, s45, v99
	v_pk_add_f32 v[98:99], v[118:119], v[74:75]
	v_pk_add_f32 v[118:119], v[120:121], v[40:41]
	v_pk_add_f32 v[120:121], v[122:123], v[76:77]
	v_pk_add_f32 v[122:123], v[56:57], v[42:43]
	s_waitcnt vmcnt(1)
	v_lshlrev_b32_e32 v56, 2, v158
	v_lshlrev_b32_e32 v106, 16, v44
	v_and_b32_e32 v107, 0xffff0000, v44
	v_lshlrev_b32_e32 v44, 16, v45
	v_and_b32_e32 v45, 0xffff0000, v45
	v_lshlrev_b32_e32 v46, 16, v47
	v_and_b32_e32 v47, 0xffff0000, v47
	v_lshlrev_b32_e32 v48, 16, v70
	v_and_b32_e32 v49, 0xffff0000, v70
	v_lshlrev_b32_e32 v148, 16, v82
	v_and_b32_e32 v149, 0xffff0000, v82
	v_lshlrev_b32_e32 v82, 16, v83
	v_and_b32_e32 v83, 0xffff0000, v83
	v_add_u32_e32 v56, s45, v56
	s_waitcnt vmcnt(0)
	v_lshlrev_b32_e32 v159, 2, v159
	v_cvt_pk_f32_fp8_e32 v[130:131], v60
	v_cvt_pk_f32_fp8_sdwa v[60:61], v61 src0_sel:WORD_1
	v_pk_add_f32 v[106:107], v[124:125], v[106:107]
	v_pk_add_f32 v[124:125], v[126:127], v[44:45]
	v_pk_add_f32 v[126:127], v[58:59], v[46:47]
	ds_read_b32 v158, v56
	v_pk_add_f32 v[58:59], v[52:53], v[48:49]
	v_pk_add_f32 v[52:53], v[152:153], v[82:83]
	v_add_u32_e32 v82, s45, v159
	v_lshlrev_b32_e32 v112, 16, v50
	v_and_b32_e32 v113, 0xffff0000, v50
	v_lshlrev_b32_e32 v116, 16, v54
	v_and_b32_e32 v117, 0xffff0000, v54
	v_lshlrev_b32_e32 v54, 16, v55
	v_and_b32_e32 v55, 0xffff0000, v55
	ds_read_b32 v82, v82
	v_pk_add_f32 v[112:113], v[134:135], v[112:113]
	v_pk_add_f32 v[134:135], v[62:63], v[54:55]
	v_cvt_pk_f32_fp8_sdwa v[54:55], v91 src0_sel:WORD_1
	v_cvt_pk_f32_fp8_e32 v[150:151], v96
	v_cvt_pk_f32_fp8_e32 v[156:157], v97
	v_cvt_pk_f32_fp8_sdwa v[96:97], v97 src0_sel:WORD_1
	v_lshlrev_b32_e32 v50, 16, v51
	v_and_b32_e32 v51, 0xffff0000, v51
	v_ashrrev_i32_e32 v41, 31, v100
	v_mov_b32_e32 v40, v100
	v_ashrrev_i32_e32 v43, 31, v101
	v_mov_b32_e32 v42, v101
	v_pk_add_f32 v[110:111], v[130:131], v[110:111]
	v_pk_add_f32 v[130:131], v[60:61], v[50:51]
	v_pk_add_f32 v[114:115], v[136:137], v[114:115]
	v_lshlrev_b64 v[76:77], 11, v[40:41]
	v_lshlrev_b64 v[74:75], 11, v[42:43]
	v_lshlrev_b32_e32 v40, 16, v68
	v_and_b32_e32 v41, 0xffff0000, v68
	v_lshlrev_b32_e32 v42, 16, v69
	v_and_b32_e32 v43, 0xffff0000, v69
	v_lshlrev_b32_e32 v50, 16, v71
	v_and_b32_e32 v51, 0xffff0000, v71
	v_cvt_pk_f32_fp8_e32 v[68:69], v92
	v_cvt_pk_f32_fp8_sdwa v[70:71], v92 src0_sel:WORD_1
	v_cvt_pk_f32_fp8_e32 v[136:137], v93
	v_cvt_pk_f32_fp8_sdwa v[142:143], v94 src0_sel:WORD_1
	v_lshlrev_b32_e32 v154, 16, v84
	v_and_b32_e32 v155, 0xffff0000, v84
	v_lshlrev_b32_e32 v84, 16, v85
	v_and_b32_e32 v85, 0xffff0000, v85
	s_waitcnt lgkmcnt(1)
	v_ashrrev_i32_e32 v159, 31, v158
	v_pk_add_f32 v[116:117], v[140:141], v[116:117]
	v_cvt_pk_f32_fp8_e32 v[44:45], v90
	v_cvt_pk_f32_fp8_sdwa v[46:47], v90 src0_sel:WORD_1
	v_lshlrev_b32_e32 v90, 16, v66
	v_and_b32_e32 v91, 0xffff0000, v66
	v_lshlrev_b32_e32 v100, 16, v67
	v_and_b32_e32 v101, 0xffff0000, v67
	v_cvt_pk_f32_fp8_e32 v[140:141], v94
	v_cvt_pk_f32_fp8_e32 v[146:147], v95
	v_cvt_pk_f32_fp8_sdwa v[94:95], v95 src0_sel:WORD_1
	v_pk_add_f32 v[66:67], v[54:55], v[50:51]
	v_pk_add_f32 v[54:55], v[96:97], v[84:85]
	v_lshlrev_b64 v[84:85], 19, v[158:159]
	s_waitcnt lgkmcnt(0)
	v_ashrrev_i32_e32 v83, 31, v82
	v_lshlrev_b32_e32 v60, 16, v64
	v_and_b32_e32 v61, 0xffff0000, v64
	v_lshlrev_b32_e32 v62, 16, v65
	v_and_b32_e32 v63, 0xffff0000, v65
	v_cvt_pk_f32_fp8_sdwa v[92:93], v93 src0_sel:WORD_1
	v_lshl_add_u64 v[84:85], s[18:19], 0, v[84:85]
	v_lshlrev_b64 v[82:83], 19, v[82:83]
	v_lshlrev_b32_e32 v138, 16, v86
	v_and_b32_e32 v139, 0xffff0000, v86
	v_lshlrev_b32_e32 v86, 16, v87
	v_and_b32_e32 v87, 0xffff0000, v87
	v_pk_add_f32 v[60:61], v[68:69], v[60:61]
	v_pk_add_f32 v[68:69], v[70:71], v[62:63]
	v_pk_add_f32 v[62:63], v[136:137], v[90:91]
	v_lshl_add_u64 v[84:85], v[84:85], 0, v[104:105]
	v_lshl_add_u64 v[90:91], s[18:19], 0, v[82:83]
	v_lshlrev_b32_e32 v144, 16, v88
	v_and_b32_e32 v145, 0xffff0000, v88
	v_lshlrev_b32_e32 v88, 16, v89
	v_and_b32_e32 v89, 0xffff0000, v89
	v_pk_add_f32 v[48:49], v[142:143], v[86:87]
	v_lshl_add_u64 v[86:87], v[84:85], 0, v[36:37]
	v_lshl_add_u64 v[90:91], v[90:91], 0, v[102:103]
	v_pk_add_f32 v[50:51], v[94:95], v[88:89]
	global_load_dwordx4 v[82:85], v[86:87], off
	s_nop 0
	global_load_dwordx4 v[86:89], v[86:87], off offset:1024
	v_lshl_add_u64 v[94:95], v[90:91], 0, v[36:37]
	v_pk_add_f32 v[70:71], v[92:93], v[100:101]
	global_load_dwordx4 v[90:93], v[94:95], off
	s_nop 0
	global_load_dwordx4 v[94:97], v[94:95], off offset:1024
	ds_read_b32 v220, v178
	ds_read_b32 v222, v179
	s_waitcnt lgkmcnt(0)
	v_ashrrev_i32_e32 v221, 31, v220
	v_ashrrev_i32_e32 v223, 31, v222
	v_lshlrev_b64 v[220:221], 19, v[220:221]
	v_lshlrev_b64 v[222:223], 19, v[222:223]
	v_lshl_add_u64 v[220:221], s[18:19], 0, v[220:221]
	v_lshl_add_u64 v[222:223], s[18:19], 0, v[222:223]
	v_lshl_add_u64 v[220:221], v[220:221], 0, v[76:77]
	v_lshl_add_u64 v[222:223], v[222:223], 0, v[74:75]
	v_lshl_add_u64 v[220:221], v[220:221], 0, v[36:37]
	v_lshl_add_u64 v[222:223], v[222:223], 0, v[36:37]
	global_load_dwordx4 v[224:227], v[220:221], off
	global_load_dwordx4 v[228:231], v[222:223], off
	global_load_dwordx4 v[232:235], v[220:221], off offset:1024
	global_load_dwordx4 v[236:239], v[222:223], off offset:1024
	v_pk_add_f32 v[56:57], v[44:45], v[40:41]
	v_pk_add_f32 v[40:41], v[140:141], v[138:139]
	v_pk_add_f32 v[64:65], v[46:47], v[42:43]
	v_pk_add_f32 v[42:43], v[146:147], v[144:145]
	v_pk_add_f32 v[44:45], v[150:151], v[148:149]
	v_pk_add_f32 v[46:47], v[156:157], v[154:155]
	s_waitcnt vmcnt(7)
	v_cvt_pk_f32_fp8_e32 v[100:101], v82
	v_cvt_pk_f32_fp8_sdwa v[102:103], v82 src0_sel:WORD_1
	v_cvt_pk_f32_fp8_e32 v[104:105], v83
	v_cvt_pk_f32_fp8_sdwa v[82:83], v83 src0_sel:WORD_1
	v_cvt_pk_f32_fp8_e32 v[136:137], v84
	v_cvt_pk_f32_fp8_sdwa v[138:139], v84 src0_sel:WORD_1
	v_cvt_pk_f32_fp8_e32 v[140:141], v85
	v_cvt_pk_f32_fp8_sdwa v[84:85], v85 src0_sel:WORD_1
	s_waitcnt vmcnt(6)
	v_cvt_pk_f32_fp8_e32 v[142:143], v86
	v_cvt_pk_f32_fp8_sdwa v[144:145], v86 src0_sel:WORD_1
	v_cvt_pk_f32_fp8_e32 v[146:147], v87
	v_cvt_pk_f32_fp8_sdwa v[86:87], v87 src0_sel:WORD_1
	v_cvt_pk_f32_fp8_e32 v[148:149], v88
	v_cvt_pk_f32_fp8_sdwa v[150:151], v88 src0_sel:WORD_1
	v_cvt_pk_f32_fp8_e32 v[152:153], v89
	v_cvt_pk_f32_fp8_sdwa v[88:89], v89 src0_sel:WORD_1
	s_waitcnt vmcnt(5)
	v_cvt_pk_f32_fp8_e32 v[154:155], v90
	v_cvt_pk_f32_fp8_sdwa v[156:157], v90 src0_sel:WORD_1
	v_cvt_pk_f32_fp8_e32 v[158:159], v91
	v_cvt_pk_f32_fp8_sdwa v[90:91], v91 src0_sel:WORD_1
	v_cvt_pk_f32_fp8_e32 v[160:161], v92
	v_cvt_pk_f32_fp8_sdwa v[162:163], v92 src0_sel:WORD_1
	v_cvt_pk_f32_fp8_e32 v[164:165], v93
	v_cvt_pk_f32_fp8_sdwa v[92:93], v93 src0_sel:WORD_1
	s_waitcnt vmcnt(4)
	v_cvt_pk_f32_fp8_e32 v[166:167], v94
	v_cvt_pk_f32_fp8_sdwa v[168:169], v94 src0_sel:WORD_1
	v_cvt_pk_f32_fp8_e32 v[170:171], v95
	v_cvt_pk_f32_fp8_sdwa v[94:95], v95 src0_sel:WORD_1
	v_cvt_pk_f32_fp8_e32 v[172:173], v96
	v_cvt_pk_f32_fp8_sdwa v[174:175], v96 src0_sel:WORD_1
	v_cvt_pk_f32_fp8_e32 v[176:177], v97
	v_cvt_pk_f32_fp8_sdwa v[96:97], v97 src0_sel:WORD_1
	v_pk_mul_f32 v[102:103], v[72:73], v[102:103] op_sel:[1,0]
	v_pk_mul_f32 v[100:101], v[72:73], v[100:101] op_sel:[1,0]
	v_pk_mul_f32 v[82:83], v[72:73], v[82:83] op_sel:[1,0]
	v_pk_mul_f32 v[104:105], v[72:73], v[104:105] op_sel:[1,0]
	v_pk_mul_f32 v[138:139], v[72:73], v[138:139] op_sel:[1,0]
	v_pk_mul_f32 v[136:137], v[72:73], v[136:137] op_sel:[1,0]
	v_pk_mul_f32 v[140:141], v[72:73], v[140:141] op_sel:[1,0]
	v_pk_mul_f32 v[84:85], v[72:73], v[84:85] op_sel:[1,0]
	v_pk_mul_f32 v[144:145], v[72:73], v[144:145] op_sel:[1,0]
	v_pk_mul_f32 v[142:143], v[72:73], v[142:143] op_sel:[1,0]
	v_pk_mul_f32 v[86:87], v[72:73], v[86:87] op_sel:[1,0]
	v_pk_mul_f32 v[146:147], v[72:73], v[146:147] op_sel:[1,0]
	v_pk_mul_f32 v[150:151], v[72:73], v[150:151] op_sel:[1,0]
	v_pk_mul_f32 v[148:149], v[72:73], v[148:149] op_sel:[1,0]
	v_pk_mul_f32 v[88:89], v[72:73], v[88:89] op_sel:[1,0]
	v_pk_mul_f32 v[152:153], v[72:73], v[152:153] op_sel:[1,0]
	v_pk_fma_f32 v[100:101], v[72:73], v[154:155], v[100:101] op_sel_hi:[0,1,1]
	v_pk_fma_f32 v[102:103], v[72:73], v[156:157], v[102:103] op_sel_hi:[0,1,1]
	v_pk_fma_f32 v[104:105], v[72:73], v[158:159], v[104:105] op_sel_hi:[0,1,1]
	v_pk_fma_f32 v[82:83], v[72:73], v[90:91], v[82:83] op_sel_hi:[0,1,1]
	v_pk_fma_f32 v[90:91], v[72:73], v[160:161], v[136:137] op_sel_hi:[0,1,1]
	v_pk_fma_f32 v[136:137], v[72:73], v[162:163], v[138:139] op_sel_hi:[0,1,1]
	v_pk_fma_f32 v[138:139], v[72:73], v[164:165], v[140:141] op_sel_hi:[0,1,1]
	v_pk_fma_f32 v[84:85], v[72:73], v[92:93], v[84:85] op_sel_hi:[0,1,1]
	v_pk_fma_f32 v[92:93], v[72:73], v[166:167], v[142:143] op_sel_hi:[0,1,1]
	v_pk_fma_f32 v[140:141], v[72:73], v[168:169], v[144:145] op_sel_hi:[0,1,1]
	v_pk_fma_f32 v[142:143], v[72:73], v[170:171], v[146:147] op_sel_hi:[0,1,1]
	v_pk_fma_f32 v[94:95], v[72:73], v[94:95], v[86:87] op_sel_hi:[0,1,1]
	v_pk_fma_f32 v[144:145], v[72:73], v[172:173], v[148:149] op_sel_hi:[0,1,1]
	v_pk_fma_f32 v[146:147], v[72:73], v[174:175], v[150:151] op_sel_hi:[0,1,1]
	v_pk_fma_f32 v[148:149], v[72:73], v[176:177], v[152:153] op_sel_hi:[0,1,1]
	v_pk_fma_f32 v[72:73], v[72:73], v[96:97], v[88:89] op_sel_hi:[0,1,1]
	v_pk_fma_f32 v[96:97], v[30:31], v[102:103], v[118:119]
	v_pk_fma_f32 v[98:99], v[28:29], v[100:101], v[98:99]
	v_pk_fma_f32 v[102:103], v[24:25], v[104:105], v[120:121]
	v_pk_fma_f32 v[90:91], v[20:21], v[90:91], v[106:107]
	v_pk_fma_f32 v[108:109], v[16:17], v[138:139], v[108:109]
	v_pk_fma_f32 v[106:107], v[18:19], v[84:85], v[126:127]
	v_mul_f32_e32 v126, v99, v99
	v_mul_f32_e32 v127, v103, v103
	v_mov_b32_e32 v120, v91
	v_mov_b32_e32 v121, v109
	v_pk_fma_f32 v[100:101], v[26:27], v[82:83], v[122:123]
	v_pk_fma_f32 v[104:105], v[22:23], v[136:137], v[124:125]
	v_mov_b32_e32 v118, v90
	v_mov_b32_e32 v119, v108
	v_cvt_pk_bf16_f32 v16, v98, v99
	v_cvt_pk_bf16_f32 v17, v96, v97
	v_cvt_pk_bf16_f32 v18, v102, v103
	v_cvt_pk_bf16_f32 v19, v100, v101
	v_cvt_pk_bf16_f32 v20, v90, v91
	v_cvt_pk_bf16_f32 v21, v104, v105
	v_cvt_pk_bf16_f32 v22, v108, v109
	v_cvt_pk_bf16_f32 v23, v106, v107
	ds_read_b128 v[24:27], v81 offset:4096
	ds_read_b128 v[28:31], v81 offset:5120
	ds_read_b128 v[82:85], v81 offset:6144
	ds_read_b128 v[86:89], v81 offset:7168
	v_fmac_f32_e32 v126, v98, v98
	v_fmac_f32_e32 v127, v102, v102
	v_pk_mul_f32 v[120:121], v[120:121], v[120:121]
	v_mov_b32_e32 v122, v104
	v_mov_b32_e32 v123, v106
	global_store_dwordx4 v[38:39], v[16:19], off
	global_store_dwordx4 v[38:39], v[20:23], off offset:16
	v_fmac_f32_e32 v126, v96, v96
	v_fmac_f32_e32 v127, v100, v100
	v_pk_fma_f32 v[16:17], v[118:119], v[118:119], v[120:121]
	v_mov_b32_e32 v124, v105
	v_mov_b32_e32 v125, v107
	v_fmac_f32_e32 v126, v97, v97
	v_fmac_f32_e32 v127, v101, v101
	v_pk_fma_f32 v[16:17], v[122:123], v[122:123], v[16:17]
	v_add_f32_e32 v18, v126, v127
	v_pk_fma_f32 v[16:17], v[124:125], v[124:125], v[16:17]
	s_waitcnt lgkmcnt(3)
	v_pk_fma_f32 v[92:93], v[24:25], v[92:93], v[110:111]
	s_waitcnt lgkmcnt(2)
	v_pk_fma_f32 v[110:111], v[28:29], v[142:143], v[112:113]
	v_add_f32_e32 v16, v18, v16
	v_pk_fma_f32 v[118:119], v[26:27], v[140:141], v[128:129]
	v_mov_b32_e32 v26, v93
	v_mov_b32_e32 v27, v111
	v_pk_fma_f32 v[94:95], v[30:31], v[94:95], v[130:131]
	s_waitcnt lgkmcnt(1)
	v_pk_fma_f32 v[114:115], v[82:83], v[144:145], v[114:115]
	s_waitcnt lgkmcnt(0)
	v_pk_fma_f32 v[120:121], v[88:89], v[72:73], v[134:135]
	v_pk_fma_f32 v[116:117], v[86:87], v[148:149], v[116:117]
	v_add_f32_e32 v89, v16, v17
	v_mov_b32_e32 v24, v92
	v_mov_b32_e32 v25, v110
	v_cvt_pk_bf16_f32 v16, v92, v93
	v_cvt_pk_bf16_f32 v17, v118, v119
	v_cvt_pk_bf16_f32 v18, v110, v111
	v_cvt_pk_bf16_f32 v19, v94, v95
	v_pk_mul_f32 v[26:27], v[26:27], v[26:27]
	v_pk_fma_f32 v[112:113], v[84:85], v[146:147], v[132:133]
	v_mov_b32_e32 v28, v118
	v_mov_b32_e32 v29, v94
	v_mov_b32_e32 v82, v115
	v_mov_b32_e32 v83, v117
	v_cvt_pk_bf16_f32 v20, v114, v115
	v_cvt_pk_bf16_f32 v21, v112, v113
	v_cvt_pk_bf16_f32 v22, v116, v117
	v_cvt_pk_bf16_f32 v23, v120, v121
	global_store_dwordx4 v[38:39], v[16:19], off offset:2048
	global_store_dwordx4 v[38:39], v[20:23], off offset:2064
	v_mov_b32_e32 v72, v119
	v_pk_fma_f32 v[16:17], v[24:25], v[24:25], v[26:27]
	v_mov_b32_e32 v73, v95
	v_mov_b32_e32 v30, v114
	v_mov_b32_e32 v31, v116
	v_pk_mul_f32 v[82:83], v[82:83], v[82:83]
	v_pk_fma_f32 v[38:39], v[28:29], v[28:29], v[16:17]
	v_mov_b32_e32 v84, v112
	v_mov_b32_e32 v85, v120
	v_pk_fma_f32 v[18:19], v[30:31], v[30:31], v[82:83]
	v_pk_fma_f32 v[38:39], v[72:73], v[72:73], v[38:39]
	v_mov_b32_e32 v86, v113
	v_mov_b32_e32 v87, v121
	v_pk_fma_f32 v[82:83], v[84:85], v[84:85], v[18:19]
	v_add_f32_e32 v38, v89, v38
	v_pk_fma_f32 v[72:73], v[86:87], v[86:87], v[82:83]
	v_add_f32_e32 v38, v38, v39
	s_nop 0
	s_nop 0
	ds_read_b128 v[16:19], v81
	ds_read_b128 v[20:23], v81 offset:1024
	ds_read_b128 v[24:27], v81 offset:2048
	ds_read_b128 v[28:31], v81 offset:3072
	v_add_f32_e32 v38, v38, v72
	v_add_f32_e32 v38, v38, v73
	s_nop 0
	s_nop 0
	v_add_f32_dpp v82, v38, v38 quad_perm:[1,0,3,2] row_mask:0xf bank_mask:0xf bound_ctrl:1
	s_nop 0
	s_nop 0
	s_nop 0
	s_nop 0
	v_add_f32_dpp v82, v82, v82 quad_perm:[2,3,0,1] row_mask:0xf bank_mask:0xf bound_ctrl:1
	s_nop 0
	s_nop 0
	v_add_f32_dpp v82, v82, v82 row_half_mirror row_mask:0xf bank_mask:0xf bound_ctrl:1
	s_nop 0
	s_nop 0
	v_add_f32_dpp v122, v82, v82 row_mirror row_mask:0xf bank_mask:0xf bound_ctrl:1
	s_nop 0
	s_nop 0
	s_nop 0
	s_nop 0
	s_nop 0
	v_readlane_b32 s48, v122, 16
	v_readlane_b32 s49, v122, 48
	v_readlane_b32 s4, v122, 0
	v_readlane_b32 s5, v122, 32
	v_mov_b32_e32 v76, s48
	v_mov_b32_e32 v77, s49
	v_pk_add_f32 v[76:77], s[4:5], v[76:77]
	s_waitcnt vmcnt(5)
	v_cvt_pk_f32_fp8_e32 v[126:127], v234
	v_add_f32_e32 v76, v76, v77
	v_fmamk_f32 v76, v76, 0x3a000000, v79
	v_mul_f32_e32 v77, 0x4f800000, v76
	v_cmp_gt_f32_e32 vcc, s46, v76
	s_waitcnt vmcnt(4)
	v_cvt_pk_f32_fp8_e32 v[130:131], v238
	v_cvt_pk_f32_fp8_sdwa v[132:133], v238 src0_sel:WORD_1
	v_cndmask_b32_e32 v76, v76, v77, vcc
	v_sqrt_f32_e32 v77, v76
	v_cvt_pk_f32_fp8_e32 v[136:137], v239
	v_cvt_pk_f32_fp8_sdwa v[88:89], v239 src0_sel:WORD_1
	v_cvt_pk_f32_fp8_sdwa v[128:129], v234 src0_sel:WORD_1
	v_add_u32_e32 v122, -1, v77
	v_add_u32_e32 v123, 1, v77
	v_fma_f32 v124, -v122, v77, v76
	v_fma_f32 v125, -v123, v77, v76
	v_cmp_ge_f32_e64 s[4:5], 0, v124
	v_cvt_pk_f32_fp8_e32 v[134:135], v235
	v_cvt_pk_f32_fp8_sdwa v[84:85], v235 src0_sel:WORD_1
	v_cndmask_b32_e64 v77, v77, v122, s[4:5]
	v_cmp_lt_f32_e64 s[4:5], 0, v125
	v_pk_mul_f32 v[132:133], v[34:35], v[132:133] op_sel:[1,0]
	v_pk_mul_f32 v[130:131], v[34:35], v[130:131] op_sel:[1,0]
	v_cndmask_b32_e64 v77, v77, v123, s[4:5]
	v_mul_f32_e32 v122, 0x37800000, v77
	v_cndmask_b32_e32 v77, v77, v122, vcc
	v_cmp_class_f32_e32 vcc, v76, v80
	v_pk_mul_f32 v[88:89], v[34:35], v[88:89] op_sel:[1,0]
	v_pk_mul_f32 v[136:137], v[34:35], v[136:137] op_sel:[1,0]
	v_cndmask_b32_e32 v76, v77, v76, vcc
	v_div_scale_f32 v77, s[4:5], v76, v76, 1.0
	v_rcp_f32_e32 v123, v77
	v_div_scale_f32 v122, vcc, 1.0, v76, 1.0
	v_pk_fma_f32 v[84:85], v[34:35], v[84:85], v[88:89] op_sel_hi:[0,1,1]
	v_fma_f32 v124, -v77, v123, 1.0
	v_fmac_f32_e32 v123, v124, v123
	v_mul_f32_e32 v124, v122, v123
	v_fma_f32 v125, -v77, v124, v122
	v_fmac_f32_e32 v124, v125, v123
	v_fma_f32 v77, -v77, v124, v122
	v_div_fmas_f32 v77, v77, v123, v124
	v_div_fixup_f32 v76, v77, v76, 1.0
	v_pk_mul_f32 v[152:153], v[96:97], v[76:77] op_sel_hi:[1,0]
	v_pk_mul_f32 v[156:157], v[100:101], v[76:77] op_sel_hi:[1,0]
	v_pk_mul_f32 v[164:165], v[106:107], v[76:77] op_sel_hi:[1,0]
	v_pk_mul_f32 v[172:173], v[94:95], v[76:77] op_sel_hi:[1,0]
	v_pk_mul_f32 v[176:177], v[112:113], v[76:77] op_sel_hi:[1,0]
	v_cvt_pk_f32_fp8_e32 v[94:95], v228
	v_cvt_pk_f32_fp8_sdwa v[96:97], v228 src0_sel:WORD_1
	v_cvt_pk_f32_fp8_e32 v[100:101], v229
	v_cvt_pk_f32_fp8_sdwa v[72:73], v229 src0_sel:WORD_1
	v_cvt_pk_f32_fp8_e32 v[106:107], v230
	v_cvt_pk_f32_fp8_e32 v[112:113], v231
	v_pk_mul_f32 v[150:151], v[98:99], v[76:77] op_sel_hi:[1,0]
	v_pk_mul_f32 v[154:155], v[102:103], v[76:77] op_sel_hi:[1,0]
	v_pk_mul_f32 v[158:159], v[90:91], v[76:77] op_sel_hi:[1,0]
	v_pk_mul_f32 v[166:167], v[92:93], v[76:77] op_sel_hi:[1,0]
	v_pk_mul_f32 v[170:171], v[110:111], v[76:77] op_sel_hi:[1,0]
	v_cvt_pk_f32_fp8_e32 v[90:91], v224
	v_cvt_pk_f32_fp8_sdwa v[92:93], v224 src0_sel:WORD_1
	v_cvt_pk_f32_fp8_e32 v[98:99], v225
	v_cvt_pk_f32_fp8_sdwa v[36:37], v225 src0_sel:WORD_1
	v_cvt_pk_f32_fp8_e32 v[102:103], v226
	v_cvt_pk_f32_fp8_e32 v[110:111], v227
	v_pk_mul_f32 v[162:163], v[108:109], v[76:77] op_sel_hi:[1,0]
	v_cvt_pk_f32_fp8_sdwa v[108:109], v230 src0_sel:WORD_1
	v_cvt_pk_f32_fp8_sdwa v[74:75], v231 src0_sel:WORD_1
	v_pk_mul_f32 v[160:161], v[104:105], v[76:77] op_sel_hi:[1,0]
	v_pk_mul_f32 v[168:169], v[118:119], v[76:77] op_sel_hi:[1,0]
	v_pk_mul_f32 v[174:175], v[114:115], v[76:77] op_sel_hi:[1,0]
	v_pk_mul_f32 v[178:179], v[116:117], v[76:77] op_sel_hi:[1,0]
	v_pk_mul_f32 v[76:77], v[120:121], v[76:77] op_sel_hi:[1,0]
	v_cvt_pk_f32_fp8_sdwa v[104:105], v226 src0_sel:WORD_1
	v_cvt_pk_f32_fp8_sdwa v[38:39], v227 src0_sel:WORD_1
	v_cvt_pk_f32_fp8_e32 v[118:119], v236
	v_cvt_pk_f32_fp8_sdwa v[120:121], v236 src0_sel:WORD_1
	v_cvt_pk_f32_fp8_e32 v[124:125], v237
	v_cvt_pk_f32_fp8_sdwa v[86:87], v237 src0_sel:WORD_1
	v_cvt_pk_f32_fp8_e32 v[114:115], v232
	v_cvt_pk_f32_fp8_sdwa v[116:117], v232 src0_sel:WORD_1
	v_cvt_pk_f32_fp8_e32 v[122:123], v233
	v_cvt_pk_f32_fp8_sdwa v[82:83], v233 src0_sel:WORD_1
	v_pk_mul_f32 v[94:95], v[34:35], v[94:95] op_sel:[1,0]
	v_pk_mul_f32 v[72:73], v[34:35], v[72:73] op_sel:[1,0]
	v_pk_mul_f32 v[100:101], v[34:35], v[100:101] op_sel:[1,0]
	v_pk_mul_f32 v[106:107], v[34:35], v[106:107] op_sel:[1,0]
	v_pk_mul_f32 v[112:113], v[34:35], v[112:113] op_sel:[1,0]
	v_pk_fma_f32 v[90:91], v[34:35], v[90:91], v[94:95] op_sel_hi:[0,1,1]
	v_pk_fma_f32 v[94:95], v[34:35], v[98:99], v[100:101] op_sel_hi:[0,1,1]
	v_pk_fma_f32 v[36:37], v[34:35], v[36:37], v[72:73] op_sel_hi:[0,1,1]
	v_pk_fma_f32 v[72:73], v[34:35], v[102:103], v[106:107] op_sel_hi:[0,1,1]
	v_pk_fma_f32 v[98:99], v[34:35], v[110:111], v[112:113] op_sel_hi:[0,1,1]
	v_pk_mul_f32 v[96:97], v[34:35], v[96:97] op_sel:[1,0]
	v_pk_mul_f32 v[108:109], v[34:35], v[108:109] op_sel:[1,0]
	v_pk_mul_f32 v[74:75], v[34:35], v[74:75] op_sel:[1,0]
	s_waitcnt lgkmcnt(3)
	v_pk_fma_f32 v[182:183], v[16:17], v[90:91], v[56:57]
	s_waitcnt lgkmcnt(2)
	v_pk_fma_f32 v[186:187], v[20:21], v[94:95], v[58:59]
	s_waitcnt lgkmcnt(1)
	v_pk_fma_f32 v[190:191], v[24:25], v[72:73], v[60:61]
	s_waitcnt lgkmcnt(0)
	v_pk_fma_f32 v[194:195], v[28:29], v[98:99], v[62:63]
	v_pk_mul_f32 v[120:121], v[34:35], v[120:121] op_sel:[1,0]
	v_pk_mul_f32 v[118:119], v[34:35], v[118:119] op_sel:[1,0]
	v_pk_mul_f32 v[86:87], v[34:35], v[86:87] op_sel:[1,0]
	v_pk_mul_f32 v[124:125], v[34:35], v[124:125] op_sel:[1,0]
	v_pk_fma_f32 v[92:93], v[34:35], v[92:93], v[96:97] op_sel_hi:[0,1,1]
	v_pk_fma_f32 v[96:97], v[34:35], v[104:105], v[108:109] op_sel_hi:[0,1,1]
	v_pk_fma_f32 v[38:39], v[34:35], v[38:39], v[74:75] op_sel_hi:[0,1,1]
	v_pk_fma_f32 v[184:185], v[22:23], v[36:37], v[66:67]
	v_mul_f32_e32 v66, v183, v183
	v_mul_f32_e32 v67, v187, v187
	v_mov_b32_e32 v60, v191
	v_mov_b32_e32 v61, v195
	v_pk_fma_f32 v[74:75], v[34:35], v[114:115], v[118:119] op_sel_hi:[0,1,1]
	v_pk_fma_f32 v[100:101], v[34:35], v[116:117], v[120:121] op_sel_hi:[0,1,1]
	v_pk_fma_f32 v[102:103], v[34:35], v[122:123], v[124:125] op_sel_hi:[0,1,1]
	v_pk_fma_f32 v[82:83], v[34:35], v[82:83], v[86:87] op_sel_hi:[0,1,1]
	v_pk_fma_f32 v[86:87], v[34:35], v[126:127], v[130:131] op_sel_hi:[0,1,1]
	v_pk_fma_f32 v[104:105], v[34:35], v[128:129], v[132:133] op_sel_hi:[0,1,1]
	v_pk_fma_f32 v[106:107], v[34:35], v[134:135], v[136:137] op_sel_hi:[0,1,1]
	v_pk_fma_f32 v[180:181], v[18:19], v[92:93], v[64:65]
	v_pk_fma_f32 v[188:189], v[26:27], v[96:97], v[68:69]
	v_pk_fma_f32 v[192:193], v[30:31], v[38:39], v[70:71]
	v_mov_b32_e32 v38, v190
	v_mov_b32_e32 v39, v194
	v_cvt_pk_bf16_f32 v16, v182, v183
	v_cvt_pk_bf16_f32 v17, v180, v181
	v_cvt_pk_bf16_f32 v18, v186, v187
	v_cvt_pk_bf16_f32 v19, v184, v185
	v_cvt_pk_bf16_f32 v20, v190, v191
	v_cvt_pk_bf16_f32 v21, v188, v189
	v_cvt_pk_bf16_f32 v22, v194, v195
	v_cvt_pk_bf16_f32 v23, v192, v193
	ds_read_b128 v[24:27], v81 offset:4096
	ds_read_b128 v[28:31], v81 offset:5120
	ds_read_b128 v[34:37], v81 offset:6144
	ds_read_b128 v[56:59], v81 offset:7168
	v_fmac_f32_e32 v66, v182, v182
	v_fmac_f32_e32 v67, v186, v186
	v_pk_mul_f32 v[60:61], v[60:61], v[60:61]
	v_mov_b32_e32 v62, v188
	v_mov_b32_e32 v63, v192
	global_store_dwordx4 v[32:33], v[16:19], off
	global_store_dwordx4 v[32:33], v[20:23], off offset:16
	v_fmac_f32_e32 v66, v180, v180
	v_fmac_f32_e32 v67, v184, v184
	v_pk_fma_f32 v[16:17], v[38:39], v[38:39], v[60:61]
	v_mov_b32_e32 v64, v189
	v_mov_b32_e32 v65, v193
	v_fmac_f32_e32 v66, v181, v181
	v_fmac_f32_e32 v67, v185, v185
	v_pk_fma_f32 v[16:17], v[62:63], v[62:63], v[16:17]
	v_add_f32_e32 v18, v66, v67
	v_pk_fma_f32 v[16:17], v[64:65], v[64:65], v[16:17]
	s_waitcnt lgkmcnt(3)
	v_pk_fma_f32 v[198:199], v[24:25], v[74:75], v[40:41]
	s_waitcnt lgkmcnt(2)
	v_pk_fma_f32 v[202:203], v[28:29], v[102:103], v[42:43]
	v_add_f32_e32 v16, v18, v16
	v_pk_fma_f32 v[196:197], v[26:27], v[100:101], v[48:49]
	v_mov_b32_e32 v26, v199
	v_mov_b32_e32 v27, v203
	v_pk_fma_f32 v[200:201], v[30:31], v[82:83], v[50:51]
	s_waitcnt lgkmcnt(1)
	v_pk_fma_f32 v[206:207], v[34:35], v[86:87], v[44:45]
	s_waitcnt lgkmcnt(0)
	v_pk_fma_f32 v[210:211], v[56:57], v[106:107], v[46:47]
	v_add_f32_e32 v81, v16, v17
	v_mov_b32_e32 v24, v198
	v_mov_b32_e32 v25, v202
	v_cvt_pk_bf16_f32 v16, v198, v199
	v_cvt_pk_bf16_f32 v17, v196, v197
	v_cvt_pk_bf16_f32 v18, v202, v203
	v_cvt_pk_bf16_f32 v19, v200, v201
	v_cvt_pk_bf16_f32 v20, v206, v207
	v_pk_mul_f32 v[26:27], v[26:27], v[26:27]
	v_pk_fma_f32 v[204:205], v[36:37], v[104:105], v[52:53]
	v_pk_fma_f32 v[208:209], v[58:59], v[84:85], v[54:55]
	v_mov_b32_e32 v28, v196
	v_mov_b32_e32 v29, v200
	v_mov_b32_e32 v36, v207
	v_mov_b32_e32 v37, v211
	v_cvt_pk_bf16_f32 v21, v204, v205
	v_cvt_pk_bf16_f32 v22, v210, v211
	v_cvt_pk_bf16_f32 v23, v208, v209
	global_store_dwordx4 v[32:33], v[16:19], off offset:2048
	global_store_dwordx4 v[32:33], v[20:23], off offset:2064
	v_mov_b32_e32 v30, v197
	v_pk_fma_f32 v[16:17], v[24:25], v[24:25], v[26:27]
	v_mbcnt_lo_u32_b32 v20, -1, 0
	v_mbcnt_hi_u32_b32 v20, -1, v20
	v_mov_b32_e32 v31, v201
	v_mov_b32_e32 v34, v206
	v_mov_b32_e32 v35, v210
	v_pk_mul_f32 v[36:37], v[36:37], v[36:37]
	v_lshlrev_b32_e32 v20, 4, v20
	v_pk_fma_f32 v[16:17], v[28:29], v[28:29], v[16:17]
	v_mov_b32_e32 v38, v204
	v_mov_b32_e32 v39, v208
	v_pk_fma_f32 v[18:19], v[34:35], v[34:35], v[36:37]
	v_ashrrev_i32_e32 v21, 31, v20
	v_pk_fma_f32 v[212:213], v[30:31], v[30:31], v[16:17]
	v_mov_b32_e32 v40, v205
	v_mov_b32_e32 v41, v209
	v_pk_fma_f32 v[18:19], v[38:39], v[38:39], v[18:19]
	v_add_u32_e32 v82, s27, v20
	v_lshl_add_u64 v[88:89], s[30:31], 0, v[20:21]
	v_add_f32_e32 v81, v81, v212
	v_pk_fma_f32 v[214:215], v[40:41], v[40:41], v[18:19]
	v_lshl_add_u64 v[86:87], s[16:17], 0, v[20:21]
	v_add_u32_e32 v90, 0x10000, v82
	v_add_u32_e32 v98, 0x10400, v82
	v_add_u32_e32 v106, 0x10800, v82
	v_add_u32_e32 v114, 0x10c00, v82
	v_add_u32_e32 v122, 0x11000, v82
	v_add_u32_e32 v130, 0x11400, v82
	v_add_u32_e32 v138, 0x11800, v82
	v_add_u32_e32 v146, 0x11c00, v82
	v_add_co_u32_e32 v216, vcc, s47, v88
	v_add_f32_e32 v81, v81, v213
	ds_read_b128 v[16:19], v82 offset:32768
	ds_read_b128 v[20:23], v82 offset:32768
	ds_read_b128 v[24:27], v82 offset:33792
	ds_read_b128 v[28:31], v82 offset:33792
	ds_read_b128 v[32:35], v82 offset:34816
	ds_read_b128 v[36:39], v82 offset:34816
	ds_read_b128 v[40:43], v82 offset:35840
	ds_read_b128 v[44:47], v82 offset:35840
	ds_read_b128 v[48:51], v82 offset:36864
	ds_read_b128 v[52:55], v82 offset:36864
	ds_read_b128 v[56:59], v82 offset:37888
	ds_read_b128 v[60:63], v82 offset:37888
	ds_read_b128 v[64:67], v82 offset:38912
	ds_read_b128 v[68:71], v82 offset:38912
	ds_read_b128 v[72:75], v82 offset:39936
	ds_read_b128 v[82:85], v82 offset:39936
	v_addc_co_u32_e32 v217, vcc, 0, v89, vcc
	v_lshl_add_u64 v[218:219], v[86:87], 0, s[34:35]
	ds_read_b128 v[86:89], v90
	ds_read_b128 v[90:93], v90
	ds_read_b128 v[94:97], v98
	ds_read_b128 v[98:101], v98
	ds_read_b128 v[102:105], v106
	ds_read_b128 v[106:109], v106
	ds_read_b128 v[110:113], v114
	ds_read_b128 v[114:117], v114
	ds_read_b128 v[118:121], v122
	ds_read_b128 v[122:125], v122
	ds_read_b128 v[126:129], v130
	ds_read_b128 v[130:133], v130
	ds_read_b128 v[134:137], v138
	ds_read_b128 v[138:141], v138
	ds_read_b128 v[142:145], v146
	ds_read_b128 v[146:149], v146
	v_add_f32_e32 v81, v81, v214
	v_add_f32_e32 v81, v81, v215
	s_waitcnt lgkmcnt(14)
	v_pk_fma_f32 v[16:17], v[150:151], v[16:17], v[86:87]
	s_waitcnt lgkmcnt(1)
	v_pk_fma_f32 v[74:75], v[76:77], v[74:75], v[144:145]
	v_add_f32_dpp v81, v81, v81 quad_perm:[1,0,3,2] row_mask:0xf bank_mask:0xf bound_ctrl:1
	v_cvt_pk_fp8_f32 v0, v16, v17
	v_pk_fma_f32 v[18:19], v[152:153], v[18:19], v[88:89]
	v_add_f32_dpp v81, v81, v81 quad_perm:[2,3,0,1] row_mask:0xf bank_mask:0xf bound_ctrl:1
	v_pk_fma_f32 v[24:25], v[154:155], v[24:25], v[94:95]
	v_cvt_pk_fp8_f32 v0, v18, v19 op_sel:[0,0,1]
	v_add_f32_dpp v76, v81, v81 row_half_mirror row_mask:0xf bank_mask:0xf bound_ctrl:1
	v_cvt_pk_fp8_f32 v1, v24, v25
	v_pk_fma_f32 v[32:33], v[158:159], v[32:33], v[102:103]
	v_add_f32_dpp v16, v76, v76 row_mirror row_mask:0xf bank_mask:0xf bound_ctrl:1
	v_pk_fma_f32 v[40:41], v[162:163], v[40:41], v[110:111]
	v_readlane_b32 s27, v16, 16
	v_readlane_b32 s30, v16, 48
	v_readlane_b32 s4, v16, 0
	v_readlane_b32 s5, v16, 32
	v_mov_b32_e32 v16, s27
	v_mov_b32_e32 v17, s30
	v_pk_add_f32 v[16:17], s[4:5], v[16:17]
	v_pk_fma_f32 v[48:49], v[166:167], v[48:49], v[118:119]
	v_add_f32_e32 v16, v16, v17
	v_fmamk_f32 v16, v16, 0x3a000000, v79
	v_mul_f32_e32 v17, 0x4f800000, v16
	v_cmp_gt_f32_e32 vcc, s46, v16
	v_pk_fma_f32 v[56:57], v[170:171], v[56:57], v[126:127]
	v_pk_fma_f32 v[64:65], v[174:175], v[64:65], v[134:135]
	v_cndmask_b32_e32 v16, v16, v17, vcc
	v_sqrt_f32_e32 v17, v16
	v_pk_fma_f32 v[72:73], v[178:179], v[72:73], v[142:143]
	v_cvt_pk_fp8_f32 v2, v32, v33
	v_cvt_pk_fp8_f32 v3, v40, v41
	v_add_u32_e32 v18, -1, v17
	v_add_u32_e32 v19, 1, v17
	v_fma_f32 v24, -v18, v17, v16
	v_fma_f32 v25, -v19, v17, v16
	v_cmp_ge_f32_e64 s[4:5], 0, v24
	v_cvt_pk_fp8_f32 v4, v48, v49
	v_cvt_pk_fp8_f32 v5, v56, v57
	v_cndmask_b32_e64 v17, v17, v18, s[4:5]
	v_cmp_lt_f32_e64 s[4:5], 0, v25
	v_cvt_pk_fp8_f32 v6, v64, v65
	v_cvt_pk_fp8_f32 v7, v72, v73
	v_cndmask_b32_e64 v17, v17, v19, s[4:5]
	v_mul_f32_e32 v18, 0x37800000, v17
	v_cndmask_b32_e32 v17, v17, v18, vcc
	v_cmp_class_f32_e32 vcc, v16, v80
	v_pk_fma_f32 v[26:27], v[156:157], v[26:27], v[96:97]
	v_pk_fma_f32 v[34:35], v[160:161], v[34:35], v[104:105]
	v_cndmask_b32_e32 v16, v17, v16, vcc
	v_div_scale_f32 v17, s[4:5], v16, v16, 1.0
	v_rcp_f32_e32 v19, v17
	v_div_scale_f32 v18, vcc, 1.0, v16, 1.0
	v_pk_fma_f32 v[42:43], v[164:165], v[42:43], v[112:113]
	v_fma_f32 v24, -v17, v19, 1.0
	v_fmac_f32_e32 v19, v24, v19
	v_mul_f32_e32 v24, v18, v19
	v_fma_f32 v25, -v17, v24, v18
	v_fmac_f32_e32 v24, v25, v19
	v_fma_f32 v17, -v17, v24, v18
	v_div_fmas_f32 v17, v17, v19, v24
	v_div_fixup_f32 v16, v17, v16, 1.0
	v_pk_fma_f32 v[50:51], v[168:169], v[50:51], v[120:121]
	v_pk_fma_f32 v[58:59], v[172:173], v[58:59], v[128:129]
	v_pk_fma_f32 v[66:67], v[176:177], v[66:67], v[136:137]
	v_cvt_pk_fp8_f32 v1, v26, v27 op_sel:[0,0,1]
	v_cvt_pk_fp8_f32 v2, v34, v35 op_sel:[0,0,1]
	v_cvt_pk_fp8_f32 v3, v42, v43 op_sel:[0,0,1]
	v_pk_mul_f32 v[18:19], v[182:183], v[16:17] op_sel_hi:[1,0]
	v_pk_mul_f32 v[24:25], v[180:181], v[16:17] op_sel_hi:[1,0]
	v_pk_mul_f32 v[26:27], v[186:187], v[16:17] op_sel_hi:[1,0]
	v_pk_mul_f32 v[32:33], v[184:185], v[16:17] op_sel_hi:[1,0]
	v_pk_mul_f32 v[34:35], v[190:191], v[16:17] op_sel_hi:[1,0]
	v_pk_mul_f32 v[42:43], v[194:195], v[16:17] op_sel_hi:[1,0]
	v_cvt_pk_fp8_f32 v4, v50, v51 op_sel:[0,0,1]
	v_cvt_pk_fp8_f32 v5, v58, v59 op_sel:[0,0,1]
	v_cvt_pk_fp8_f32 v6, v66, v67 op_sel:[0,0,1]
	v_cvt_pk_fp8_f32 v7, v74, v75 op_sel:[0,0,1]
	v_pk_mul_f32 v[40:41], v[188:189], v[16:17] op_sel_hi:[1,0]
	v_pk_mul_f32 v[48:49], v[192:193], v[16:17] op_sel_hi:[1,0]
	v_pk_mul_f32 v[50:51], v[198:199], v[16:17] op_sel_hi:[1,0]
	v_pk_mul_f32 v[58:59], v[202:203], v[16:17] op_sel_hi:[1,0]
	v_pk_mul_f32 v[66:67], v[206:207], v[16:17] op_sel_hi:[1,0]
	v_pk_mul_f32 v[74:75], v[210:211], v[16:17] op_sel_hi:[1,0]
	v_pk_fma_f32 v[22:23], v[24:25], v[22:23], v[92:93]
	v_pk_fma_f32 v[18:19], v[18:19], v[20:21], v[90:91]
	v_pk_fma_f32 v[20:21], v[32:33], v[30:31], v[100:101]
	v_pk_fma_f32 v[24:25], v[26:27], v[28:29], v[98:99]
	v_pk_fma_f32 v[28:29], v[34:35], v[36:37], v[106:107]
	v_pk_fma_f32 v[32:33], v[42:43], v[44:45], v[114:115]
	v_pk_fma_f32 v[26:27], v[40:41], v[38:39], v[108:109]
	v_pk_fma_f32 v[30:31], v[48:49], v[46:47], v[116:117]
	v_pk_fma_f32 v[36:37], v[50:51], v[52:53], v[122:123]
	v_pk_fma_f32 v[40:41], v[58:59], v[60:61], v[130:131]
	v_pk_fma_f32 v[44:45], v[66:67], v[68:69], v[138:139]
	s_waitcnt lgkmcnt(0)
	v_pk_fma_f32 v[46:47], v[74:75], v[82:83], v[146:147]
	v_cvt_pk_fp8_f32 v8, v18, v19
	v_cvt_pk_fp8_f32 v9, v24, v25
	v_cvt_pk_fp8_f32 v10, v28, v29
	v_cvt_pk_fp8_f32 v11, v32, v33
	v_cvt_pk_fp8_f32 v12, v36, v37
	v_cvt_pk_fp8_f32 v13, v40, v41
	v_cvt_pk_fp8_f32 v14, v44, v45
	v_cvt_pk_fp8_f32 v15, v46, v47
	v_pk_mul_f32 v[56:57], v[196:197], v[16:17] op_sel_hi:[1,0]
	v_pk_mul_f32 v[64:65], v[200:201], v[16:17] op_sel_hi:[1,0]
	v_pk_mul_f32 v[72:73], v[204:205], v[16:17] op_sel_hi:[1,0]
	v_pk_mul_f32 v[16:17], v[208:209], v[16:17] op_sel_hi:[1,0]
	v_pk_fma_f32 v[34:35], v[56:57], v[54:55], v[124:125]
	v_pk_fma_f32 v[38:39], v[64:65], v[62:63], v[132:133]
	v_pk_fma_f32 v[42:43], v[72:73], v[70:71], v[140:141]
	v_pk_fma_f32 v[16:17], v[16:17], v[84:85], v[148:149]
	v_cvt_pk_fp8_f32 v8, v22, v23 op_sel:[0,0,1]
	v_cvt_pk_fp8_f32 v9, v20, v21 op_sel:[0,0,1]
	v_cvt_pk_fp8_f32 v10, v26, v27 op_sel:[0,0,1]
	v_cvt_pk_fp8_f32 v11, v30, v31 op_sel:[0,0,1]
	v_cvt_pk_fp8_f32 v12, v34, v35 op_sel:[0,0,1]
	v_cvt_pk_fp8_f32 v13, v38, v39 op_sel:[0,0,1]
	v_cvt_pk_fp8_f32 v14, v42, v43 op_sel:[0,0,1]
	v_cvt_pk_fp8_f32 v15, v16, v17 op_sel:[0,0,1]
	global_store_dwordx4 v[216:217], v[0:3], off
	global_store_dwordx4 v[216:217], v[4:7], off offset:1024
	global_store_dwordx4 v[218:219], v[8:11], off
	global_store_dwordx4 v[218:219], v[12:15], off offset:1024
	s_cbranch_scc1 .LBB0_3130
